# speedup vs baseline: 1.0385x; 1.0071x over previous
.LBB3_3:
	s_load_dwordx4 s[12:15], s[0:1], 0x70
	s_load_dwordx2 s[20:21], s[0:1], 0x80
	v_and_b32_e32 v1, 15, v0
	s_and_b32 s30, s6, 56
	s_and_b32 s11, s11, 48
	s_andn2_b64 vcc, exec, s[4:5]
	v_bfe_u32 v158, v0, 4, 2
	s_cbranch_vccnz .LBB3_82
	s_bfe_u32 s4, s24, 0x10006
	s_lshl_b32 s5, s4, 4
	s_ashr_i32 s2, s3, 31
	s_mul_i32 s17, s3, 40
	s_mul_hi_i32 s16, s3, 40
	s_add_u32 s22, s0, s17
	s_addc_u32 s23, s1, s16
	s_load_dwordx4 s[16:19], s[22:23], 0x0
	s_load_dwordx2 s[0:1], s[22:23], 0x10
	v_or_b32_e32 v159, s5, v1
	v_lshlrev_b32_e32 v18, 5, v159
	s_waitcnt lgkmcnt(0)
	global_load_dwordx4 v[230:233], v18, s[18:19]
	global_load_dwordx4 v[234:237], v18, s[0:1]
	global_load_dwordx4 v[238:241], v18, s[18:19] offset:16
	global_load_dwordx4 v[242:245], v18, s[0:1] offset:16
	v_bfe_u32 v21, v0, 7, 1
	v_lshrrev_b32_e32 v19, 4, v0
	v_lshrrev_b32_e32 v20, 6, v0
	v_lshlrev_b16_e32 v24, 2, v21
	v_lshrrev_b32_e32 v18, 5, v0
	s_movk_i32 s0, 0x3000
	v_and_b32_e32 v23, 4, v20
	v_and_b32_e32 v25, 3, v19
	v_lshlrev_b32_e32 v20, 12, v20
	v_lshlrev_b32_e32 v21, 11, v21
	v_bitop3_b16 v19, v24, v19, 3 bitop3:0xf8
	s_bitcmp1_b32 s24, 6
	v_and_b32_e32 v18, 4, v18
	v_or3_b32 v163, v20, v21, s0
	v_and_b32_e32 v19, 0xffff, v19
	s_cselect_b64 s[24:25], -1, 0
	s_lshl_b32 s0, s6, 6
	v_or_b32_e32 v161, v18, v158
	v_add_u32_e32 v162, s30, v23
	v_bitop3_b16 v24, v24, 8, v25 bitop3:0xfe
	v_lshlrev_b32_e32 v25, 3, v23
	v_lshl_or_b32 v23, v23, 12, v21
	v_bitop3_b32 v18, v18, v159, v158 bitop3:0x36
	v_bitop3_b32 v19, s5, v19, v1 bitop3:0x36
	s_lshl_b32 s31, s7, 12
	s_and_b32 s0, s0, 0xe00
	s_movk_i32 s1, 0x2000
	v_and_b32_e32 v22, 0x100, v0
	v_lshl_or_b32 v168, v18, 4, v23
	v_lshlrev_b32_e32 v18, 4, v19
	s_or_b32 s0, s31, s0
	v_add3_u32 v170, v23, v18, s1
	v_or_b32_e32 v18, s0, v22
	v_or_b32_e32 v18, s11, v18
	s_movk_i32 s26, 0x600
	v_add_u32_e32 v18, v161, v18
	v_mul_lo_u32 v18, v18, s26
	v_and_b32_e32 v20, 0xffff, v24
	v_lshl_or_b32 v18, s4, 8, v18
	v_lshlrev_b32_e32 v160, 9, v158
	v_bitop3_b32 v20, s5, v20, v1 bitop3:0x36
	v_lshl_or_b32 v18, v1, 4, v18
	v_add_u32_e32 v164, -1, v162
	v_add_u32_e32 v165, 4, v162
	v_or3_b32 v166, v161, v25, 8
	v_or_b32_e32 v167, 0x1000, v23
	v_lshl_or_b32 v169, v20, 4, v160
	s_and_b32 s17, s17, 0xffff
	s_mov_b32 s19, 0x20000
	s_mov_b32 s18, 0x1800000
	v_add_u32_e32 v171, 0xfffe7c00, v18
	s_mov_b32 s33, s11
	s_mov_b32 s93, 0
	s_branch .LBB3_7

.LBB3_7:
	v_add_u32_e32 v182, s33, v161
	v_add_u32_e32 v181, -1, v182
	v_or_b32_e32 v2, v181, v164
	v_add_u32_e32 v180, 0x18400, v171
	v_cmp_gt_u32_e64 s[0:1], 64, v2
	s_mov_b64 s[4:5], -1
	s_and_b64 vcc, exec, s[24:25]
	s_cbranch_vccz .LBB3_45
	s_load_dwordx2 s[4:5], s[22:23], 0x20
	s_waitcnt lgkmcnt(0)
	s_load_dwordx2 s[26:27], s[4:5], 0x0
	s_load_dword s34, s[4:5], 0x8
	v_cmp_lt_u32_e64 s[64:65], 0, v182
	v_cmp_gt_u32_e64 s[66:67], 63, v182
	v_cmp_lt_u32_e64 s[68:69], 0, v162
	v_cmp_gt_u32_e64 s[70:71], 60, v162
	buffer_load_dwordx4 v[186:189], v180, s[16:19], 0 offen
	s_and_b64 s[72:73], s[68:69], s[64:65]
	s_and_b64 s[74:75], s[68:69], s[66:67]
	s_and_b64 s[76:77], s[70:71], s[64:65]
	s_and_b64 s[78:79], s[70:71], s[66:67]
	v_add_u32_e32 v249, 0xfffe7c00, v180
	v_add_u32_e32 v250, 0xfffe8000, v180
	s_mov_b64 exec, s[72:73]
	buffer_load_dwordx4 v[110:113], v249, s[16:19], 0 offen
	buffer_load_dwordx4 v[70:73], v249, s[16:19], 0 offen offset:512
	s_mov_b64 exec, -1
	s_mov_b64 exec, s[68:69]
	buffer_load_dwordx4 v[126:129], v250, s[16:19], 0 offen offset:512
	buffer_load_dwordx4 v[98:101], v250, s[16:19], 0 offen offset:1024
	s_mov_b64 exec, -1
	s_mov_b64 exec, s[74:75]
	buffer_load_dwordx4 v[134:137], v250, s[16:19], 0 offen offset:2048
	buffer_load_dwordx4 v[114:117], v250, s[16:19], 0 offen offset:2560
	s_mov_b64 exec, -1
	v_add_u32_e32 v249, 0xfffffc00, v180
	s_mov_b64 exec, s[64:65]
	buffer_load_dwordx4 v[82:85], v249, s[16:19], 0 offen
	buffer_load_dwordx4 v[42:45], v249, s[16:19], 0 offen offset:512
	s_mov_b64 exec, -1
	buffer_load_dwordx4 v[106:109], v180, s[16:19], 0 offen offset:512
	buffer_load_dwordx4 v[62:65], v180, s[16:19], 0 offen offset:1024
	s_mov_b64 exec, s[66:67]
	buffer_load_dwordx4 v[122:125], v180, s[16:19], 0 offen offset:2048
	buffer_load_dwordx4 v[86:89], v180, s[16:19], 0 offen offset:2560
	s_mov_b64 exec, -1
	v_add_u32_e32 v249, 0x17c00, v180
	v_add_u32_e32 v250, 0x18000, v180
	s_mov_b64 exec, s[64:65]
	buffer_load_dwordx4 v[50:53], v249, s[16:19], 0 offen
	buffer_load_dwordx4 v[22:25], v249, s[16:19], 0 offen offset:512
	s_mov_b64 exec, -1
	buffer_load_dwordx4 v[66:69], v250, s[16:19], 0 offen offset:512
	buffer_load_dwordx4 v[30:33], v250, s[16:19], 0 offen offset:1024
	s_mov_b64 exec, s[66:67]
	buffer_load_dwordx4 v[94:97], v250, s[16:19], 0 offen offset:2048
	buffer_load_dwordx4 v[46:49], v250, s[16:19], 0 offen offset:2560
	s_mov_b64 exec, -1
	v_add_u32_e32 v249, 0x18000, v180
	buffer_load_dwordx4 v[154:157], v249, s[16:19], 0 offen
	v_add_u32_e32 v250, 0x30000, v180
	buffer_load_dwordx4 v[150:153], v250, s[16:19], 0 offen
	v_add_u32_e32 v249, 0x48000, v180
	buffer_load_dwordx4 v[146:149], v249, s[16:19], 0 offen
	v_add_u32_e32 v249, 0x2fc00, v180
	v_add_u32_e32 v250, 0x30000, v180
	v_add_u32_e32 v251, 0x47c00, v180
	v_add_u32_e32 v252, 0x48000, v180
	v_add_u32_e32 v253, 0x5fc00, v180
	v_add_u32_e32 v254, 0x60000, v180
	s_cmp_lg_u32 s93, 0
	s_cbranch_scc1 .Lmybg_B1
	s_waitcnt vmcnt(22)
	v_cvt_pk_f16_f32 v172, v230, v231
	v_cvt_pk_f16_f32 v173, v234, v235
	v_cvt_pk_f16_f32 v174, v232, v233
	v_cvt_pk_f16_f32 v175, v236, v237
	v_cvt_pk_f16_f32 v176, v238, v239
	v_cvt_pk_f16_f32 v177, v242, v243
	v_cvt_pk_f16_f32 v178, v240, v241
	v_cvt_pk_f16_f32 v179, v244, v245
	s_mov_b32 s93, 1
.Lmybg_B1:
	s_not_b64 exec, s[72:73]
	s_cbranch_execz .Lmyf_B1_0
	v_mov_b32_e32 v110, v172
	v_mov_b32_e32 v111, v174
	v_mov_b32_e32 v112, v176
	v_mov_b32_e32 v113, v178
	v_mov_b32_e32 v70, v173
	v_mov_b32_e32 v71, v175
	v_mov_b32_e32 v72, v177
	v_mov_b32_e32 v73, v179

.LBB3_45:
	s_and_b64 vcc, exec, s[4:5]
	s_cbranch_vccz .LBB3_6
	s_load_dwordx2 s[0:1], s[22:23], 0x18
	s_waitcnt lgkmcnt(0)
	s_load_dwordx2 s[6:7], s[0:1], 0x0
	s_load_dword s28, s[0:1], 0x8
	v_cmp_lt_u32_e64 s[64:65], 0, v182
	v_cmp_gt_u32_e64 s[66:67], 63, v182
	v_cmp_lt_u32_e64 s[68:69], 0, v162
	v_cmp_gt_u32_e64 s[70:71], 60, v162
	buffer_load_dwordx4 v[184:187], v180, s[16:19], 0 offen
	s_and_b64 s[72:73], s[68:69], s[64:65]
	s_and_b64 s[74:75], s[68:69], s[66:67]
	s_and_b64 s[76:77], s[70:71], s[64:65]
	s_and_b64 s[78:79], s[70:71], s[66:67]
	v_add_u32_e32 v249, 0xfffe7c00, v180
	v_add_u32_e32 v250, 0xfffe8000, v180
	s_mov_b64 exec, s[72:73]
	buffer_load_dwordx4 v[110:113], v249, s[16:19], 0 offen
	buffer_load_dwordx4 v[78:81], v249, s[16:19], 0 offen offset:512
	s_mov_b64 exec, -1
	s_mov_b64 exec, s[68:69]
	buffer_load_dwordx4 v[126:129], v250, s[16:19], 0 offen offset:512
	buffer_load_dwordx4 v[102:105], v250, s[16:19], 0 offen offset:1024
	s_mov_b64 exec, -1
	s_mov_b64 exec, s[74:75]
	buffer_load_dwordx4 v[138:141], v250, s[16:19], 0 offen offset:2048
	buffer_load_dwordx4 v[118:121], v250, s[16:19], 0 offen offset:2560
	s_mov_b64 exec, -1
	v_add_u32_e32 v249, 0xfffffc00, v180
	s_mov_b64 exec, s[64:65]
	buffer_load_dwordx4 v[86:89], v249, s[16:19], 0 offen
	buffer_load_dwordx4 v[46:49], v249, s[16:19], 0 offen offset:512
	s_mov_b64 exec, -1
	buffer_load_dwordx4 v[106:109], v180, s[16:19], 0 offen offset:512
	buffer_load_dwordx4 v[62:65], v180, s[16:19], 0 offen offset:1024
	s_mov_b64 exec, s[66:67]
	buffer_load_dwordx4 v[122:125], v180, s[16:19], 0 offen offset:2048
	buffer_load_dwordx4 v[82:85], v180, s[16:19], 0 offen offset:2560
	s_mov_b64 exec, -1
	v_add_u32_e32 v249, 0x17c00, v180
	v_add_u32_e32 v250, 0x18000, v180
	s_mov_b64 exec, s[64:65]
	buffer_load_dwordx4 v[50:53], v249, s[16:19], 0 offen
	buffer_load_dwordx4 v[22:25], v249, s[16:19], 0 offen offset:512
	s_mov_b64 exec, -1
	buffer_load_dwordx4 v[66:69], v250, s[16:19], 0 offen offset:512
	buffer_load_dwordx4 v[34:37], v250, s[16:19], 0 offen offset:1024
	s_mov_b64 exec, s[66:67]
	buffer_load_dwordx4 v[94:97], v250, s[16:19], 0 offen offset:2048
	buffer_load_dwordx4 v[42:45], v250, s[16:19], 0 offen offset:2560
	s_mov_b64 exec, -1
	v_add_u32_e32 v249, 0x18000, v180
	buffer_load_dwordx4 v[154:157], v249, s[16:19], 0 offen
	v_add_u32_e32 v250, 0x30000, v180
	buffer_load_dwordx4 v[150:153], v250, s[16:19], 0 offen
	v_add_u32_e32 v249, 0x48000, v180
	buffer_load_dwordx4 v[146:149], v249, s[16:19], 0 offen
	v_add_u32_e32 v249, 0x2fc00, v180
	v_add_u32_e32 v250, 0x30000, v180
	v_add_u32_e32 v251, 0x47c00, v180
	v_add_u32_e32 v252, 0x48000, v180
	v_add_u32_e32 v253, 0x5fc00, v180
	v_add_u32_e32 v254, 0x60000, v180
	s_cmp_lg_u32 s93, 0
	s_cbranch_scc1 .Lmybg_B2
	s_waitcnt vmcnt(22)
	v_cvt_pk_f16_f32 v172, v230, v231
	v_cvt_pk_f16_f32 v173, v234, v235
	v_cvt_pk_f16_f32 v174, v232, v233
	v_cvt_pk_f16_f32 v175, v236, v237
	v_cvt_pk_f16_f32 v176, v238, v239
	v_cvt_pk_f16_f32 v177, v242, v243
	v_cvt_pk_f16_f32 v178, v240, v241
	v_cvt_pk_f16_f32 v179, v244, v245
	s_mov_b32 s93, 1
.Lmybg_B2:
	s_not_b64 exec, s[72:73]
	s_cbranch_execz .Lmyf_B2_0
	v_mov_b32_e32 v110, v172
	v_mov_b32_e32 v111, v174
	v_mov_b32_e32 v112, v176
	v_mov_b32_e32 v113, v178
	v_mov_b32_e32 v78, v173
	v_mov_b32_e32 v79, v175
	v_mov_b32_e32 v80, v177
	v_mov_b32_e32 v81, v179

.LBB4_4:
	global_load_dwordx4 v[2:5], v[170:171], off
	global_load_dwordx4 v[8:11], v[172:173], off
	global_load_dwordx4 v[210:213], v[170:171], off offset:16
	global_load_dwordx4 v[214:217], v[172:173], off offset:16
	s_lshl_b32 s48, s46, 3
	s_add_i32 s48, s48, s44
	v_or_b32_e32 v199, s48, v178
	v_add_u32_e32 v168, v199, v181
	v_add_u32_e32 v201, -1, v199
	v_mul_lo_u32 v6, v168, s47
	v_or_b32_e32 v7, v201, v182
	v_or_b32_e32 v6, v6, v166
	s_mov_b64 s[4:5], -1
	s_and_b64 vcc, exec, s[26:27]
	v_cmp_gt_u32_e64 s[2:3], 64, v7
	v_lshlrev_b32_e32 v200, 1, v6
	s_cbranch_vccz .LBB4_42
	global_load_dwordx3 v[154:156], v169, s[10:11]
	v_cmp_lt_u32_e64 s[64:65], 0, v199
	v_cmp_gt_u32_e64 s[66:67], 63, v199
	v_cmp_lt_u32_e64 s[68:69], 0, v180
	v_cmp_gt_u32_e64 s[70:71], 60, v180
	buffer_load_dwordx4 v[206:209], v200, s[36:39], 0 offen
	s_and_b64 s[72:73], s[68:69], s[64:65]
	s_and_b64 s[74:75], s[68:69], s[66:67]
	s_and_b64 s[76:77], s[70:71], s[64:65]
	s_and_b64 s[78:79], s[70:71], s[66:67]
	v_add_u32_e32 v245, 0xfffe7c00, v200
	v_add_u32_e32 v246, 0xfffe8000, v200
	s_mov_b64 exec, s[72:73]
	buffer_load_dwordx4 v[122:125], v245, s[36:39], 0 offen
	buffer_load_dwordx4 v[82:85], v245, s[36:39], 0 offen offset:512
	s_mov_b64 exec, -1
	s_mov_b64 exec, s[68:69]
	buffer_load_dwordx4 v[138:141], v246, s[36:39], 0 offen offset:512
	buffer_load_dwordx4 v[106:109], v246, s[36:39], 0 offen offset:1024
	s_mov_b64 exec, -1
	s_mov_b64 exec, s[74:75]
	buffer_load_dwordx4 v[146:149], v246, s[36:39], 0 offen offset:2048
	buffer_load_dwordx4 v[126:129], v246, s[36:39], 0 offen offset:2560
	s_mov_b64 exec, -1
	v_add_u32_e32 v245, 0xfffffc00, v200
	s_mov_b64 exec, s[64:65]
	buffer_load_dwordx4 v[94:97], v245, s[36:39], 0 offen
	buffer_load_dwordx4 v[54:57], v245, s[36:39], 0 offen offset:512
	s_mov_b64 exec, -1
	buffer_load_dwordx4 v[118:121], v200, s[36:39], 0 offen offset:512
	buffer_load_dwordx4 v[74:77], v200, s[36:39], 0 offen offset:1024
	s_mov_b64 exec, s[66:67]
	buffer_load_dwordx4 v[134:137], v200, s[36:39], 0 offen offset:2048
	buffer_load_dwordx4 v[98:101], v200, s[36:39], 0 offen offset:2560
	s_mov_b64 exec, -1
	v_add_u32_e32 v245, 0x17c00, v200
	v_add_u32_e32 v246, 0x18000, v200
	s_mov_b64 exec, s[64:65]
	buffer_load_dwordx4 v[62:65], v245, s[36:39], 0 offen
	buffer_load_dwordx4 v[30:33], v245, s[36:39], 0 offen offset:512
	s_mov_b64 exec, -1
	buffer_load_dwordx4 v[78:81], v246, s[36:39], 0 offen offset:512
	buffer_load_dwordx4 v[42:45], v246, s[36:39], 0 offen offset:1024
	s_mov_b64 exec, s[66:67]
	buffer_load_dwordx4 v[102:105], v246, s[36:39], 0 offen offset:2048
	buffer_load_dwordx4 v[58:61], v246, s[36:39], 0 offen offset:2560
	s_mov_b64 exec, -1
	v_add_u32_e32 v245, 0x18000, v200
	buffer_load_dwordx4 v[162:165], v245, s[36:39], 0 offen
	v_add_u32_e32 v246, 0x30000, v200
	buffer_load_dwordx4 v[158:161], v246, s[36:39], 0 offen
	v_add_u32_e32 v245, 0x2fc00, v200
	v_add_u32_e32 v246, 0x30000, v200
	v_add_u32_e32 v247, 0x47c00, v200
	v_add_u32_e32 v248, 0x48000, v200
	v_add_u32_e32 v249, 0x5fc00, v200
	v_add_u32_e32 v250, 0x60000, v200
	s_waitcnt vmcnt(22)
	v_cvt_pk_f16_f32 v6, v2, v3
	v_cvt_pk_f16_f32 v2, v8, v9
	v_cvt_pk_f16_f32 v7, v4, v5
	v_cvt_pk_f16_f32 v3, v10, v11
	v_cvt_pk_f16_f32 v8, v210, v211
	v_cvt_pk_f16_f32 v4, v214, v215
	v_cvt_pk_f16_f32 v9, v212, v213
	v_cvt_pk_f16_f32 v5, v216, v217
	s_not_b64 exec, s[72:73]
	s_cbranch_execz .Lmyf_C1_0
	v_mov_b32_e32 v122, v6
	v_mov_b32_e32 v123, v7
	v_mov_b32_e32 v124, v8
	v_mov_b32_e32 v125, v9
	v_mov_b32_e32 v82, v2
	v_mov_b32_e32 v83, v3
	v_mov_b32_e32 v84, v4
	v_mov_b32_e32 v85, v5

.LBB4_42:
	s_and_b64 vcc, exec, s[4:5]
	s_cbranch_vccz .LBB4_80
	global_load_dwordx3 v[146:148], v169, s[8:9]
	v_cmp_lt_u32_e64 s[64:65], 0, v199
	v_cmp_gt_u32_e64 s[66:67], 63, v199
	v_cmp_lt_u32_e64 s[68:69], 0, v180
	v_cmp_gt_u32_e64 s[70:71], 60, v180
	buffer_load_dwordx4 v[162:165], v200, s[36:39], 0 offen
	s_and_b64 s[72:73], s[68:69], s[64:65]
	s_and_b64 s[74:75], s[68:69], s[66:67]
	s_and_b64 s[76:77], s[70:71], s[64:65]
	s_and_b64 s[78:79], s[70:71], s[66:67]
	v_add_u32_e32 v245, 0xfffe7c00, v200
	v_add_u32_e32 v246, 0xfffe8000, v200
	s_mov_b64 exec, s[72:73]
	buffer_load_dwordx4 v[114:117], v245, s[36:39], 0 offen
	buffer_load_dwordx4 v[74:77], v245, s[36:39], 0 offen offset:512
	s_mov_b64 exec, -1
	s_mov_b64 exec, s[68:69]
	buffer_load_dwordx4 v[130:133], v246, s[36:39], 0 offen offset:512
	buffer_load_dwordx4 v[98:101], v246, s[36:39], 0 offen offset:1024
	s_mov_b64 exec, -1
	s_mov_b64 exec, s[74:75]
	buffer_load_dwordx4 v[138:141], v246, s[36:39], 0 offen offset:2048
	buffer_load_dwordx4 v[118:121], v246, s[36:39], 0 offen offset:2560
	s_mov_b64 exec, -1
	v_add_u32_e32 v245, 0xfffffc00, v200
	s_mov_b64 exec, s[64:65]
	buffer_load_dwordx4 v[86:89], v245, s[36:39], 0 offen
	buffer_load_dwordx4 v[46:49], v245, s[36:39], 0 offen offset:512
	s_mov_b64 exec, -1
	buffer_load_dwordx4 v[110:113], v200, s[36:39], 0 offen offset:512
	buffer_load_dwordx4 v[66:69], v200, s[36:39], 0 offen offset:1024
	s_mov_b64 exec, s[66:67]
	buffer_load_dwordx4 v[126:129], v200, s[36:39], 0 offen offset:2048
	buffer_load_dwordx4 v[90:93], v200, s[36:39], 0 offen offset:2560
	s_mov_b64 exec, -1
	v_add_u32_e32 v245, 0x17c00, v200
	v_add_u32_e32 v246, 0x18000, v200
	s_mov_b64 exec, s[64:65]
	buffer_load_dwordx4 v[54:57], v245, s[36:39], 0 offen
	buffer_load_dwordx4 v[22:25], v245, s[36:39], 0 offen offset:512
	s_mov_b64 exec, -1
	buffer_load_dwordx4 v[70:73], v246, s[36:39], 0 offen offset:512
	buffer_load_dwordx4 v[34:37], v246, s[36:39], 0 offen offset:1024
	s_mov_b64 exec, s[66:67]
	buffer_load_dwordx4 v[94:97], v246, s[36:39], 0 offen offset:2048
	buffer_load_dwordx4 v[50:53], v246, s[36:39], 0 offen offset:2560
	s_mov_b64 exec, -1
	v_add_u32_e32 v245, 0x18000, v200
	buffer_load_dwordx4 v[154:157], v245, s[36:39], 0 offen
	v_add_u32_e32 v246, 0x30000, v200
	buffer_load_dwordx4 v[150:153], v246, s[36:39], 0 offen
	v_add_u32_e32 v245, 0x2fc00, v200
	v_add_u32_e32 v246, 0x30000, v200
	v_add_u32_e32 v247, 0x47c00, v200
	v_add_u32_e32 v248, 0x48000, v200
	v_add_u32_e32 v249, 0x5fc00, v200
	v_add_u32_e32 v250, 0x60000, v200
	s_waitcnt vmcnt(22)
	v_cvt_pk_f16_f32 v6, v2, v3
	v_cvt_pk_f16_f32 v2, v8, v9
	v_cvt_pk_f16_f32 v7, v4, v5
	v_cvt_pk_f16_f32 v3, v10, v11
	v_cvt_pk_f16_f32 v8, v210, v211
	v_cvt_pk_f16_f32 v4, v214, v215
	v_cvt_pk_f16_f32 v9, v212, v213
	v_cvt_pk_f16_f32 v5, v216, v217
	s_not_b64 exec, s[72:73]
	s_cbranch_execz .Lmyf_C2_0
	v_mov_b32_e32 v114, v6
	v_mov_b32_e32 v115, v7
	v_mov_b32_e32 v116, v8
	v_mov_b32_e32 v117, v9
	v_mov_b32_e32 v74, v2
	v_mov_b32_e32 v75, v3
	v_mov_b32_e32 v76, v4
	v_mov_b32_e32 v77, v5

.LBB4_80:
	v_lshlrev_b64 v[6:7], 9, v[168:169]
	v_or_b32_e32 v6, v6, v198
	v_lshl_add_u64 v[2:3], s[20:21], 0, v[6:7]
	global_load_dwordx4 v[2:5], v[2:3], off nt
	v_lshl_add_u64 v[6:7], s[22:23], 0, v[6:7]
	global_load_dwordx4 v[6:9], v[6:7], off nt
	v_add_u32_e32 v168, v185, v199
	v_lshlrev_b64 v[26:27], 9, v[168:169]
	v_or_b32_e32 v26, v26, v198
	v_lshl_add_u64 v[22:23], s[20:21], 0, v[26:27]
	global_load_dwordx4 v[22:25], v[22:23], off nt
	v_lshl_add_u64 v[26:27], s[22:23], 0, v[26:27]
	global_load_dwordx4 v[26:29], v[26:27], off nt
	v_pk_add_f16 v17, v17, v33
	v_pk_add_f16 v16, v16, v32
	v_pk_add_f16 v15, v15, v31
	v_pk_add_f16 v14, v14, v30
	v_pk_fma_f16 v42, v13, v33, v21
	v_pk_fma_f16 v43, v12, v32, v20
	v_rcp_f16_e32 v12, v14
	v_rcp_f16_sdwa v13, v14 dst_sel:DWORD dst_unused:UNUSED_PAD src0_sel:WORD_1
	v_rcp_f16_e32 v14, v15
	v_rcp_f16_sdwa v15, v15 dst_sel:DWORD dst_unused:UNUSED_PAD src0_sel:WORD_1
	v_rcp_f16_e32 v46, v16
	v_rcp_f16_sdwa v16, v16 dst_sel:DWORD dst_unused:UNUSED_PAD src0_sel:WORD_1
	v_rcp_f16_e32 v47, v17
	v_rcp_f16_sdwa v17, v17 dst_sel:DWORD dst_unused:UNUSED_PAD src0_sel:WORD_1
	v_add_u32_e32 v168, v187, v199
	v_pk_fma_f16 v44, v10, v30, v18
	v_pk_fma_f16 v45, v11, v31, v19
	v_lshlrev_b64 v[10:11], 9, v[168:169]
	v_or_b32_e32 v10, v10, v198
	v_lshl_add_u64 v[38:39], s[20:21], 0, v[10:11]
	v_lshl_add_u64 v[40:41], s[22:23], 0, v[10:11]
	v_pack_b32_f16 v48, v14, v15
	v_pack_b32_f16 v49, v12, v13
	v_pack_b32_f16 v46, v46, v16
	v_pack_b32_f16 v47, v47, v17
	global_load_dwordx4 v[10:13], v[38:39], off nt
	global_load_dwordx4 v[14:17], v[40:41], off nt
	v_cvt_f32_f16_sdwa v21, v139 dst_sel:DWORD dst_unused:UNUSED_PAD src0_sel:WORD_1
	v_cvt_f32_f16_e32 v20, v139
	v_cvt_f32_f16_sdwa v19, v138 dst_sel:DWORD dst_unused:UNUSED_PAD src0_sel:WORD_1
	v_cvt_f32_f16_e32 v18, v138
	v_cvt_f32_f16_sdwa v33, v141 dst_sel:DWORD dst_unused:UNUSED_PAD src0_sel:WORD_1
	v_cvt_f32_f16_e32 v32, v141
	v_pk_mul_f16 v58, v43, v46
	v_pk_mul_f16 v59, v42, v47
	v_cvt_f32_f16_sdwa v31, v140 dst_sel:DWORD dst_unused:UNUSED_PAD src0_sel:WORD_1
	v_cvt_f32_f16_e32 v30, v140
	v_pk_mul_f16 v52, v45, v48
	v_pk_mul_f16 v53, v44, v49
	v_add_u32_e32 v168, v190, v199
	v_lshlrev_b64 v[36:37], 9, v[168:169]
	v_or_b32_e32 v36, v36, v198
	v_lshl_or_b32 v50, s46, 6, v178
	v_lshlrev_b32_e32 v51, 9, v50
	v_add_u32_e32 v203, v184, v51
	v_cvt_f32_f16_sdwa v35, v77 dst_sel:DWORD dst_unused:UNUSED_PAD src0_sel:WORD_1
	v_cvt_f32_f16_e32 v34, v77
	v_add_lshl_u32 v202, v188, v50, 9
	s_mov_b64 s[4:5], -1
	s_and_b64 vcc, exec, s[26:27]
	s_waitcnt vmcnt(5)
	v_cvt_f32_f16_e32 v38, v2
	v_cvt_f32_f16_sdwa v39, v2 dst_sel:DWORD dst_unused:UNUSED_PAD src0_sel:WORD_1
	v_cvt_f32_f16_e32 v2, v3
	v_cvt_f32_f16_sdwa v3, v3 dst_sel:DWORD dst_unused:UNUSED_PAD src0_sel:WORD_1
	s_waitcnt vmcnt(4)
	v_cvt_f32_f16_e32 v40, v6
	v_cvt_f32_f16_sdwa v41, v6 dst_sel:DWORD dst_unused:UNUSED_PAD src0_sel:WORD_1
	v_cvt_f32_f16_e32 v6, v7
	v_cvt_f32_f16_sdwa v7, v7 dst_sel:DWORD dst_unused:UNUSED_PAD src0_sel:WORD_1
	v_cvt_f32_f16_e32 v42, v4
	v_cvt_f32_f16_sdwa v43, v4 dst_sel:DWORD dst_unused:UNUSED_PAD src0_sel:WORD_1
	v_cvt_f32_f16_e32 v4, v5
	v_cvt_f32_f16_sdwa v5, v5 dst_sel:DWORD dst_unused:UNUSED_PAD src0_sel:WORD_1
	v_cvt_f32_f16_e32 v44, v8
	v_cvt_f32_f16_sdwa v45, v8 dst_sel:DWORD dst_unused:UNUSED_PAD src0_sel:WORD_1
	v_cvt_f32_f16_e32 v8, v9
	v_cvt_f32_f16_sdwa v9, v9 dst_sel:DWORD dst_unused:UNUSED_PAD src0_sel:WORD_1
	v_pk_add_f32 v[2:3], v[20:21], v[2:3]
	v_pk_add_f32 v[18:19], v[18:19], v[38:39]
	v_pk_add_f32 v[4:5], v[32:33], v[4:5]
	v_pk_add_f32 v[6:7], v[2:3], v[6:7]
	v_pk_add_f32 v[20:21], v[30:31], v[42:43]
	v_pk_add_f32 v[18:19], v[18:19], v[40:41]
	v_pk_add_f32 v[8:9], v[4:5], v[8:9]
	v_cvt_pk_f16_f32 v3, v6, v7
	v_lshl_add_u64 v[6:7], s[20:21], 0, v[36:37]
	v_pk_add_f32 v[20:21], v[20:21], v[44:45]
	v_cvt_pk_f16_f32 v2, v18, v19
	v_cvt_pk_f16_f32 v5, v8, v9
	global_load_dwordx4 v[6:9], v[6:7], off nt
	v_lshl_add_u64 v[18:19], s[22:23], 0, v[36:37]
	v_cvt_pk_f16_f32 v4, v20, v21
	global_load_dwordx4 v[18:21], v[18:19], off nt
	s_waitcnt vmcnt(5)
	v_cvt_f32_f16_e32 v46, v22
	v_cvt_f32_f16_sdwa v47, v22 dst_sel:DWORD dst_unused:UNUSED_PAD src0_sel:WORD_1
	ds_write_b128 v203, v[2:5]
	v_cvt_f32_f16_sdwa v5, v76 dst_sel:DWORD dst_unused:UNUSED_PAD src0_sel:WORD_1
	v_cvt_f32_f16_e32 v4, v76
	v_cvt_f32_f16_e32 v22, v23
	v_cvt_f32_f16_sdwa v23, v23 dst_sel:DWORD dst_unused:UNUSED_PAD src0_sel:WORD_1
	s_waitcnt vmcnt(4)
	v_cvt_f32_f16_e32 v48, v26
	v_cvt_f32_f16_sdwa v49, v26 dst_sel:DWORD dst_unused:UNUSED_PAD src0_sel:WORD_1
	v_cvt_f32_f16_e32 v26, v27
	v_cvt_f32_f16_sdwa v27, v27 dst_sel:DWORD dst_unused:UNUSED_PAD src0_sel:WORD_1
	v_cvt_f32_f16_sdwa v31, v75 dst_sel:DWORD dst_unused:UNUSED_PAD src0_sel:WORD_1
	v_cvt_f32_f16_e32 v30, v75
	v_cvt_f32_f16_e32 v32, v24
	v_cvt_f32_f16_sdwa v33, v24 dst_sel:DWORD dst_unused:UNUSED_PAD src0_sel:WORD_1
	v_pk_add_f32 v[4:5], v[4:5], v[22:23]
	v_cvt_f32_f16_e32 v22, v28
	v_pk_add_f32 v[4:5], v[4:5], v[26:27]
	v_cvt_f32_f16_sdwa v23, v28 dst_sel:DWORD dst_unused:UNUSED_PAD src0_sel:WORD_1
	v_cvt_f32_f16_sdwa v27, v74 dst_sel:DWORD dst_unused:UNUSED_PAD src0_sel:WORD_1
	v_cvt_f32_f16_e32 v26, v74
	v_cvt_f32_f16_e32 v24, v25
	v_cvt_f32_f16_sdwa v25, v25 dst_sel:DWORD dst_unused:UNUSED_PAD src0_sel:WORD_1
	v_pk_add_f32 v[2:3], v[34:35], v[46:47]
	v_cvt_f32_f16_e32 v28, v29
	v_cvt_f32_f16_sdwa v29, v29 dst_sel:DWORD dst_unused:UNUSED_PAD src0_sel:WORD_1
	v_pk_add_f32 v[2:3], v[2:3], v[48:49]
	s_nop 0
	v_cvt_pk_f16_f32 v2, v2, v3
	v_cvt_pk_f16_f32 v3, v4, v5
	v_pk_add_f32 v[4:5], v[30:31], v[32:33]
	s_nop 0
	v_pk_add_f32 v[4:5], v[4:5], v[22:23]
	v_pk_add_f32 v[22:23], v[26:27], v[24:25]
	v_cvt_pk_f16_f32 v4, v4, v5
	v_pk_add_f32 v[22:23], v[22:23], v[28:29]
	s_waitcnt vmcnt(3)
	v_cvt_f32_f16_e32 v24, v10
	v_cvt_pk_f16_f32 v5, v22, v23
	v_add_u32_e32 v22, v186, v50
	v_lshlrev_b32_e32 v204, 9, v22
	v_bitop3_b32 v22, v22, v179, 15 bitop3:0x6c
	v_lshlrev_b32_e32 v205, 4, v22
	v_cvt_f32_f16_sdwa v25, v10 dst_sel:DWORD dst_unused:UNUSED_PAD src0_sel:WORD_1
	v_or_b32_e32 v10, v205, v204
	v_cvt_f32_f16_sdwa v23, v57 dst_sel:DWORD dst_unused:UNUSED_PAD src0_sel:WORD_1
	v_cvt_f32_f16_e32 v22, v57
	ds_write_b128 v10, v[2:5]
	v_cvt_f32_f16_sdwa v5, v56 dst_sel:DWORD dst_unused:UNUSED_PAD src0_sel:WORD_1
	v_cvt_f32_f16_e32 v4, v56
	v_cvt_f32_f16_e32 v10, v11
	v_cvt_f32_f16_sdwa v11, v11 dst_sel:DWORD dst_unused:UNUSED_PAD src0_sel:WORD_1
	s_waitcnt vmcnt(2)
	v_cvt_f32_f16_e32 v26, v14
	v_cvt_f32_f16_sdwa v27, v14 dst_sel:DWORD dst_unused:UNUSED_PAD src0_sel:WORD_1
	v_cvt_f32_f16_e32 v14, v15
	v_cvt_f32_f16_sdwa v15, v15 dst_sel:DWORD dst_unused:UNUSED_PAD src0_sel:WORD_1
	v_pk_add_f32 v[2:3], v[22:23], v[24:25]
	v_cvt_f32_f16_sdwa v23, v55 dst_sel:DWORD dst_unused:UNUSED_PAD src0_sel:WORD_1
	v_cvt_f32_f16_e32 v22, v55
	v_cvt_f32_f16_e32 v24, v12
	v_cvt_f32_f16_sdwa v25, v12 dst_sel:DWORD dst_unused:UNUSED_PAD src0_sel:WORD_1
	v_pk_add_f32 v[4:5], v[4:5], v[10:11]
	v_cvt_f32_f16_e32 v10, v16
	v_pk_add_f32 v[4:5], v[4:5], v[14:15]
	v_cvt_f32_f16_sdwa v11, v16 dst_sel:DWORD dst_unused:UNUSED_PAD src0_sel:WORD_1
	v_cvt_f32_f16_sdwa v15, v54 dst_sel:DWORD dst_unused:UNUSED_PAD src0_sel:WORD_1
	v_cvt_f32_f16_e32 v14, v54
	v_cvt_f32_f16_e32 v12, v13
	v_cvt_f32_f16_sdwa v13, v13 dst_sel:DWORD dst_unused:UNUSED_PAD src0_sel:WORD_1
	v_cvt_f32_f16_e32 v16, v17
	v_cvt_f32_f16_sdwa v17, v17 dst_sel:DWORD dst_unused:UNUSED_PAD src0_sel:WORD_1
	v_pk_add_f32 v[2:3], v[2:3], v[26:27]
	s_nop 0
	v_cvt_pk_f16_f32 v2, v2, v3
	v_cvt_pk_f16_f32 v3, v4, v5
	v_pk_add_f32 v[4:5], v[22:23], v[24:25]
	s_nop 0
	v_pk_add_f32 v[4:5], v[4:5], v[10:11]
	v_pk_add_f32 v[10:11], v[14:15], v[12:13]
	v_cvt_pk_f16_f32 v4, v4, v5
	v_pk_add_f32 v[10:11], v[10:11], v[16:17]
	s_waitcnt vmcnt(1)
	v_cvt_f32_f16_e32 v12, v6
	v_cvt_pk_f16_f32 v5, v10, v11
	v_cvt_f32_f16_e32 v10, v53
	v_cvt_f32_f16_sdwa v11, v53 dst_sel:DWORD dst_unused:UNUSED_PAD src0_sel:WORD_1
	v_cvt_f32_f16_sdwa v13, v6 dst_sel:DWORD dst_unused:UNUSED_PAD src0_sel:WORD_1
	s_waitcnt vmcnt(0)
	v_cvt_f32_f16_e32 v14, v18
	v_cvt_f32_f16_sdwa v15, v18 dst_sel:DWORD dst_unused:UNUSED_PAD src0_sel:WORD_1
	v_or_b32_e32 v6, v189, v202
	ds_write_b128 v6, v[2:5]
	v_cvt_f32_f16_e32 v4, v52
	v_cvt_f32_f16_sdwa v5, v52 dst_sel:DWORD dst_unused:UNUSED_PAD src0_sel:WORD_1
	v_cvt_f32_f16_e32 v6, v7
	v_cvt_f32_f16_sdwa v7, v7 dst_sel:DWORD dst_unused:UNUSED_PAD src0_sel:WORD_1
	v_pk_add_f32 v[2:3], v[10:11], v[12:13]
	v_cvt_f32_f16_e32 v10, v19
	v_cvt_f32_f16_sdwa v11, v19 dst_sel:DWORD dst_unused:UNUSED_PAD src0_sel:WORD_1
	v_pk_add_f32 v[2:3], v[2:3], v[14:15]
	v_cvt_f32_f16_e32 v12, v58
	v_cvt_f32_f16_sdwa v13, v58 dst_sel:DWORD dst_unused:UNUSED_PAD src0_sel:WORD_1
	v_cvt_f32_f16_e32 v14, v8
	v_cvt_f32_f16_sdwa v15, v8 dst_sel:DWORD dst_unused:UNUSED_PAD src0_sel:WORD_1
	v_pk_add_f32 v[4:5], v[4:5], v[6:7]
	v_cvt_f32_f16_e32 v6, v20
	v_pk_add_f32 v[4:5], v[4:5], v[10:11]
	v_cvt_f32_f16_sdwa v7, v20 dst_sel:DWORD dst_unused:UNUSED_PAD src0_sel:WORD_1
	v_cvt_f32_f16_e32 v10, v59
	v_cvt_f32_f16_sdwa v11, v59 dst_sel:DWORD dst_unused:UNUSED_PAD src0_sel:WORD_1
	v_cvt_f32_f16_e32 v8, v9
	v_cvt_f32_f16_sdwa v9, v9 dst_sel:DWORD dst_unused:UNUSED_PAD src0_sel:WORD_1
	v_cvt_pk_f16_f32 v2, v2, v3
	v_cvt_pk_f16_f32 v3, v4, v5
	v_pk_add_f32 v[4:5], v[12:13], v[14:15]
	v_cvt_f32_f16_e32 v12, v21
	v_cvt_f32_f16_sdwa v13, v21 dst_sel:DWORD dst_unused:UNUSED_PAD src0_sel:WORD_1
	v_pk_add_f32 v[4:5], v[4:5], v[6:7]
	v_pk_add_f32 v[6:7], v[10:11], v[8:9]
	v_cvt_pk_f16_f32 v4, v4, v5
	v_pk_add_f32 v[6:7], v[6:7], v[12:13]
	s_nop 0
	v_cvt_pk_f16_f32 v5, v6, v7
	v_add_lshl_u32 v6, v191, v50, 9
	v_add_u32_e32 v168, v192, v6
	ds_write_b128 v168, v[2:5]
	global_load_dwordx4 v[2:5], v[174:175], off
	global_load_dwordx4 v[8:11], v[176:177], off
	global_load_dwordx4 v[12:15], v[174:175], off offset:16
	global_load_dwordx4 v[16:19], v[176:177], off offset:16
	s_cbranch_vccz .LBB4_118
	global_load_dwordx3 v[154:156], v169, s[18:19]
	s_mov_b32 s14, s38
	s_mov_b32 s15, s39
	v_cmp_lt_u32_e64 s[64:65], 0, v199
	v_cmp_gt_u32_e64 s[66:67], 63, v199
	v_cmp_lt_u32_e64 s[68:69], 0, v180
	v_cmp_gt_u32_e64 s[70:71], 60, v180
	buffer_load_dwordx4 v[210:213], v200, s[12:15], 0 offen
	s_and_b64 s[72:73], s[68:69], s[64:65]
	s_and_b64 s[74:75], s[68:69], s[66:67]
	s_and_b64 s[76:77], s[70:71], s[64:65]
	s_and_b64 s[78:79], s[70:71], s[66:67]
	v_add_u32_e32 v245, 0xfffe7c00, v200
	v_add_u32_e32 v246, 0xfffe8000, v200
	s_mov_b64 exec, s[72:73]
	buffer_load_dwordx4 v[122:125], v245, s[12:15], 0 offen
	buffer_load_dwordx4 v[82:85], v245, s[12:15], 0 offen offset:512
	s_mov_b64 exec, -1
	s_mov_b64 exec, s[68:69]
	buffer_load_dwordx4 v[138:141], v246, s[12:15], 0 offen offset:512
	buffer_load_dwordx4 v[106:109], v246, s[12:15], 0 offen offset:1024
	s_mov_b64 exec, -1
	s_mov_b64 exec, s[74:75]
	buffer_load_dwordx4 v[146:149], v246, s[12:15], 0 offen offset:2048
	buffer_load_dwordx4 v[126:129], v246, s[12:15], 0 offen offset:2560
	s_mov_b64 exec, -1
	v_add_u32_e32 v245, 0xfffffc00, v200
	s_mov_b64 exec, s[64:65]
	buffer_load_dwordx4 v[94:97], v245, s[12:15], 0 offen
	buffer_load_dwordx4 v[54:57], v245, s[12:15], 0 offen offset:512
	s_mov_b64 exec, -1
	buffer_load_dwordx4 v[118:121], v200, s[12:15], 0 offen offset:512
	buffer_load_dwordx4 v[74:77], v200, s[12:15], 0 offen offset:1024
	s_mov_b64 exec, s[66:67]
	buffer_load_dwordx4 v[134:137], v200, s[12:15], 0 offen offset:2048
	buffer_load_dwordx4 v[98:101], v200, s[12:15], 0 offen offset:2560
	s_mov_b64 exec, -1
	v_add_u32_e32 v245, 0x17c00, v200
	v_add_u32_e32 v246, 0x18000, v200
	s_mov_b64 exec, s[64:65]
	buffer_load_dwordx4 v[62:65], v245, s[12:15], 0 offen
	buffer_load_dwordx4 v[30:33], v245, s[12:15], 0 offen offset:512
	s_mov_b64 exec, -1
	buffer_load_dwordx4 v[78:81], v246, s[12:15], 0 offen offset:512
	buffer_load_dwordx4 v[42:45], v246, s[12:15], 0 offen offset:1024
	s_mov_b64 exec, s[66:67]
	buffer_load_dwordx4 v[102:105], v246, s[12:15], 0 offen offset:2048
	buffer_load_dwordx4 v[58:61], v246, s[12:15], 0 offen offset:2560
	s_mov_b64 exec, -1
	v_add_u32_e32 v245, 0x18000, v200
	buffer_load_dwordx4 v[162:165], v245, s[12:15], 0 offen
	v_add_u32_e32 v246, 0x30000, v200
	buffer_load_dwordx4 v[158:161], v246, s[12:15], 0 offen
	v_add_u32_e32 v245, 0x2fc00, v200
	v_add_u32_e32 v246, 0x30000, v200
	v_add_u32_e32 v247, 0x47c00, v200
	v_add_u32_e32 v248, 0x48000, v200
	v_add_u32_e32 v249, 0x5fc00, v200
	v_add_u32_e32 v250, 0x60000, v200
	s_waitcnt vmcnt(22)
	v_cvt_pk_f16_f32 v6, v2, v3
	v_cvt_pk_f16_f32 v2, v8, v9
	v_cvt_pk_f16_f32 v7, v4, v5
	v_cvt_pk_f16_f32 v3, v10, v11
	v_cvt_pk_f16_f32 v8, v12, v13
	v_cvt_pk_f16_f32 v4, v16, v17
	v_cvt_pk_f16_f32 v9, v14, v15
	v_cvt_pk_f16_f32 v5, v18, v19
	s_not_b64 exec, s[72:73]
	s_cbranch_execz .Lmyf_C3_0
	v_mov_b32_e32 v122, v6
	v_mov_b32_e32 v123, v7
	v_mov_b32_e32 v124, v8
	v_mov_b32_e32 v125, v9
	v_mov_b32_e32 v82, v2
	v_mov_b32_e32 v83, v3
	v_mov_b32_e32 v84, v4
	v_mov_b32_e32 v85, v5

.LBB4_118:
	s_and_b64 vcc, exec, s[4:5]
	s_cbranch_vccz .LBB4_3
	global_load_dwordx3 v[146:148], v169, s[16:17]
	s_mov_b32 s14, s38
	s_mov_b32 s15, s39
	v_cmp_lt_u32_e64 s[64:65], 0, v199
	v_cmp_gt_u32_e64 s[66:67], 63, v199
	v_cmp_lt_u32_e64 s[68:69], 0, v180
	v_cmp_gt_u32_e64 s[70:71], 60, v180
	buffer_load_dwordx4 v[162:165], v200, s[12:15], 0 offen
	s_and_b64 s[72:73], s[68:69], s[64:65]
	s_and_b64 s[74:75], s[68:69], s[66:67]
	s_and_b64 s[76:77], s[70:71], s[64:65]
	s_and_b64 s[78:79], s[70:71], s[66:67]
	v_add_u32_e32 v245, 0xfffe7c00, v200
	v_add_u32_e32 v246, 0xfffe8000, v200
	s_mov_b64 exec, s[72:73]
	buffer_load_dwordx4 v[114:117], v245, s[12:15], 0 offen
	buffer_load_dwordx4 v[70:73], v245, s[12:15], 0 offen offset:512
	s_mov_b64 exec, -1
	s_mov_b64 exec, s[68:69]
	buffer_load_dwordx4 v[130:133], v246, s[12:15], 0 offen offset:512
	buffer_load_dwordx4 v[94:97], v246, s[12:15], 0 offen offset:1024
	s_mov_b64 exec, -1
	s_mov_b64 exec, s[74:75]
	buffer_load_dwordx4 v[138:141], v246, s[12:15], 0 offen offset:2048
	buffer_load_dwordx4 v[118:121], v246, s[12:15], 0 offen offset:2560
	s_mov_b64 exec, -1
	v_add_u32_e32 v245, 0xfffffc00, v200
	s_mov_b64 exec, s[64:65]
	buffer_load_dwordx4 v[86:89], v245, s[12:15], 0 offen
	buffer_load_dwordx4 v[42:45], v245, s[12:15], 0 offen offset:512
	s_mov_b64 exec, -1
	buffer_load_dwordx4 v[110:113], v200, s[12:15], 0 offen offset:512
	buffer_load_dwordx4 v[66:69], v200, s[12:15], 0 offen offset:1024
	s_mov_b64 exec, s[66:67]
	buffer_load_dwordx4 v[126:129], v200, s[12:15], 0 offen offset:2048
	buffer_load_dwordx4 v[90:93], v200, s[12:15], 0 offen offset:2560
	s_mov_b64 exec, -1
	v_add_u32_e32 v245, 0x17c00, v200
	v_add_u32_e32 v246, 0x18000, v200
	s_mov_b64 exec, s[64:65]
	buffer_load_dwordx4 v[54:57], v245, s[12:15], 0 offen
	buffer_load_dwordx4 v[22:25], v245, s[12:15], 0 offen offset:512
	s_mov_b64 exec, -1
	buffer_load_dwordx4 v[74:77], v246, s[12:15], 0 offen offset:512
	buffer_load_dwordx4 v[34:37], v246, s[12:15], 0 offen offset:1024
	s_mov_b64 exec, s[66:67]
	buffer_load_dwordx4 v[98:101], v246, s[12:15], 0 offen offset:2048
	buffer_load_dwordx4 v[50:53], v246, s[12:15], 0 offen offset:2560
	s_mov_b64 exec, -1
	v_add_u32_e32 v245, 0x18000, v200
	buffer_load_dwordx4 v[154:157], v245, s[12:15], 0 offen
	v_add_u32_e32 v246, 0x30000, v200
	buffer_load_dwordx4 v[150:153], v246, s[12:15], 0 offen
	v_add_u32_e32 v245, 0x2fc00, v200
	v_add_u32_e32 v246, 0x30000, v200
	v_add_u32_e32 v247, 0x47c00, v200
	v_add_u32_e32 v248, 0x48000, v200
	v_add_u32_e32 v249, 0x5fc00, v200
	v_add_u32_e32 v250, 0x60000, v200
	s_waitcnt vmcnt(22)
	v_cvt_pk_f16_f32 v6, v2, v3
	v_cvt_pk_f16_f32 v2, v8, v9
	v_cvt_pk_f16_f32 v7, v4, v5
	v_cvt_pk_f16_f32 v3, v10, v11
	v_cvt_pk_f16_f32 v8, v12, v13
	v_cvt_pk_f16_f32 v4, v16, v17
	v_cvt_pk_f16_f32 v9, v14, v15
	v_cvt_pk_f16_f32 v5, v18, v19
	s_not_b64 exec, s[72:73]
	s_cbranch_execz .Lmyf_C4_0
	v_mov_b32_e32 v114, v6
	v_mov_b32_e32 v115, v7
	v_mov_b32_e32 v116, v8
	v_mov_b32_e32 v117, v9
	v_mov_b32_e32 v70, v2
	v_mov_b32_e32 v71, v3
	v_mov_b32_e32 v72, v4
	v_mov_b32_e32 v73, v5

_Z7k_stageILi0ELi4EEv8AttnArgsPKDF16_PKfPDF16_iii:
	v_readfirstlane_b32 s94, v0
	s_nop 0
	s_lshr_b32 s94, s94, 6
	s_load_dwordx4 s[8:11], s[0:1], 0x70
	s_load_dwordx2 s[20:21], s[0:1], 0x80
	s_load_dwordx4 s[12:15], s[0:1], 0x88
	s_lshl_b32 s5, s2, 5
	s_waitcnt lgkmcnt(0)
	s_and_b32 s15, s5, 0xe0
	s_lshr_b32 s5, s2, 3
	s_add_i32 s15, s15, s5
	s_and_b32 s2, s2, 56
	v_readfirstlane_b32 s4, v0
	v_and_b32_e32 v1, 15, v0
	s_cmp_lt_i32 s14, 1
	v_bfe_u32 v158, v0, 4, 2
	s_cbranch_scc1 .LBB5_79
	s_bfe_u32 s5, s4, 0x10006
	s_lshl_b32 s6, s5, 4
	s_mul_i32 s16, s3, 40
	s_mul_hi_i32 s7, s3, 40
	s_add_u32 s22, s0, s16
	s_addc_u32 s23, s1, s7
	s_load_dwordx4 s[16:19], s[22:23], 0x0
	s_load_dwordx2 s[0:1], s[22:23], 0x10
	v_or_b32_e32 v159, s6, v1
	v_lshlrev_b32_e32 v18, 5, v159
	s_waitcnt lgkmcnt(0)
	global_load_dwordx4 v[230:233], v18, s[18:19]
	global_load_dwordx4 v[234:237], v18, s[0:1]
	global_load_dwordx4 v[238:241], v18, s[18:19] offset:16
	global_load_dwordx4 v[242:245], v18, s[0:1] offset:16
	v_bfe_u32 v21, v0, 7, 1
	v_lshrrev_b32_e32 v19, 4, v0
	v_lshlrev_b16_e32 v23, 2, v21
	v_lshrrev_b32_e32 v18, 5, v0
	v_lshrrev_b32_e32 v20, 6, v0
	v_and_b32_e32 v24, 3, v19
	v_bitop3_b16 v19, v23, v19, 3 bitop3:0xf8
	s_movk_i32 s0, 0x3000
	v_and_b32_e32 v18, 4, v18
	v_and_b32_e32 v22, 4, v20
	v_lshlrev_b32_e32 v20, 12, v20
	v_lshlrev_b32_e32 v21, 11, v21
	v_and_b32_e32 v19, 0xffff, v19
	s_bitcmp1_b32 s4, 6
	v_or_b32_e32 v161, v18, v158
	v_and_or_b32 v162, s15, 56, v22
	v_bitop3_b16 v23, v23, 8, v24 bitop3:0xfe
	v_lshlrev_b32_e32 v24, 3, v22
	v_lshl_or_b32 v22, v22, 12, v21
	v_or3_b32 v163, v20, v21, s0
	v_bitop3_b32 v18, v18, v159, v158 bitop3:0x36
	v_bitop3_b32 v19, s6, v19, v1 bitop3:0x36
	s_cselect_b64 s[24:25], -1, 0
	s_and_b32 s0, s15, 0x1ffc0
	s_movk_i32 s1, 0x2000
	v_lshl_or_b32 v168, v18, 4, v22
	v_lshlrev_b32_e32 v18, 4, v19
	v_or_b32_e32 v19, s0, v162
	v_add3_u32 v170, v22, v18, s1
	v_lshl_or_b32 v18, v19, 6, s2
	v_add_u32_e32 v18, v161, v18
	v_mul_u32_u24_e32 v18, 0x600, v18
	v_and_b32_e32 v20, 0xffff, v23
	v_lshl_or_b32 v18, s5, 8, v18
	v_lshlrev_b32_e32 v160, 9, v158
	v_bitop3_b32 v20, s6, v20, v1 bitop3:0x36
	v_lshl_or_b32 v18, v1, 4, v18
	v_add_u32_e32 v164, -1, v162
	v_add_u32_e32 v165, 4, v162
	v_or3_b32 v166, v161, v24, 8
	v_or_b32_e32 v167, 0x1000, v22
	v_lshl_or_b32 v169, v20, 4, v160
	s_and_b32 s17, s17, 0xffff
	s_mov_b32 s19, 0x20000
	s_mov_b32 s18, 0x1800000
	v_add_u32_e32 v171, 0xfffe7c00, v18
	s_mov_b32 s30, s2
	s_mov_b32 s93, 0
	s_branch .LBB5_4

.LBB5_4:
	v_add_u32_e32 v182, s30, v161
	v_add_u32_e32 v181, -1, v182
	v_or_b32_e32 v2, v181, v164
	v_add_u32_e32 v180, 0x18400, v171
	v_cmp_gt_u32_e64 s[0:1], 64, v2
	s_mov_b64 s[4:5], -1
	s_and_b64 vcc, exec, s[24:25]
	s_cbranch_vccz .LBB5_42
	s_load_dwordx2 s[4:5], s[22:23], 0x20
	s_waitcnt lgkmcnt(0)
	s_load_dwordx2 s[26:27], s[4:5], 0x0
	s_load_dword s31, s[4:5], 0x8
	v_cmp_lt_u32_e64 s[64:65], 0, v182
	v_cmp_gt_u32_e64 s[66:67], 63, v182
	v_cmp_lt_u32_e64 s[68:69], 0, v162
	v_cmp_gt_u32_e64 s[70:71], 60, v162
	buffer_load_dwordx4 v[186:189], v180, s[16:19], 0 offen
	s_and_b64 s[72:73], s[68:69], s[64:65]
	s_and_b64 s[74:75], s[68:69], s[66:67]
	s_and_b64 s[76:77], s[70:71], s[64:65]
	s_and_b64 s[78:79], s[70:71], s[66:67]
	v_add_u32_e32 v224, 0xfffe7c00, v180
	v_add_u32_e32 v225, 0xfffe8000, v180
	s_mov_b64 exec, s[72:73]
	buffer_load_dwordx4 v[110:113], v224, s[16:19], 0 offen
	buffer_load_dwordx4 v[70:73], v224, s[16:19], 0 offen offset:512
	s_mov_b64 exec, -1
	s_mov_b64 exec, s[68:69]
	buffer_load_dwordx4 v[126:129], v225, s[16:19], 0 offen offset:512
	buffer_load_dwordx4 v[98:101], v225, s[16:19], 0 offen offset:1024
	s_mov_b64 exec, -1
	s_mov_b64 exec, s[74:75]
	buffer_load_dwordx4 v[134:137], v225, s[16:19], 0 offen offset:2048
	buffer_load_dwordx4 v[114:117], v225, s[16:19], 0 offen offset:2560
	s_mov_b64 exec, -1
	v_add_u32_e32 v224, 0xfffffc00, v180
	s_mov_b64 exec, s[64:65]
	buffer_load_dwordx4 v[82:85], v224, s[16:19], 0 offen
	buffer_load_dwordx4 v[42:45], v224, s[16:19], 0 offen offset:512
	s_mov_b64 exec, -1
	buffer_load_dwordx4 v[106:109], v180, s[16:19], 0 offen offset:512
	buffer_load_dwordx4 v[62:65], v180, s[16:19], 0 offen offset:1024
	s_mov_b64 exec, s[66:67]
	buffer_load_dwordx4 v[122:125], v180, s[16:19], 0 offen offset:2048
	buffer_load_dwordx4 v[86:89], v180, s[16:19], 0 offen offset:2560
	s_mov_b64 exec, -1
	v_add_u32_e32 v224, 0x17c00, v180
	v_add_u32_e32 v225, 0x18000, v180
	s_mov_b64 exec, s[64:65]
	buffer_load_dwordx4 v[50:53], v224, s[16:19], 0 offen
	buffer_load_dwordx4 v[22:25], v224, s[16:19], 0 offen offset:512
	s_mov_b64 exec, -1
	buffer_load_dwordx4 v[66:69], v225, s[16:19], 0 offen offset:512
	buffer_load_dwordx4 v[30:33], v225, s[16:19], 0 offen offset:1024
	s_mov_b64 exec, s[66:67]
	buffer_load_dwordx4 v[94:97], v225, s[16:19], 0 offen offset:2048
	buffer_load_dwordx4 v[46:49], v225, s[16:19], 0 offen offset:2560
	s_mov_b64 exec, -1
	v_add_u32_e32 v224, 0x18000, v180
	buffer_load_dwordx4 v[154:157], v224, s[16:19], 0 offen
	v_add_u32_e32 v225, 0x30000, v180
	buffer_load_dwordx4 v[150:153], v225, s[16:19], 0 offen
	v_add_u32_e32 v224, 0x48000, v180
	buffer_load_dwordx4 v[146:149], v224, s[16:19], 0 offen
	v_add_u32_e32 v224, 0x2fc00, v180
	v_add_u32_e32 v225, 0x30000, v180
	v_add_u32_e32 v226, 0x47c00, v180
	v_add_u32_e32 v227, 0x48000, v180
	v_add_u32_e32 v228, 0x5fc00, v180
	v_add_u32_e32 v229, 0x60000, v180
	s_cmp_lg_u32 s93, 0
	s_cbranch_scc1 .Lmybg_D1
	s_waitcnt vmcnt(22)
	v_cvt_pk_f16_f32 v172, v230, v231
	v_cvt_pk_f16_f32 v173, v234, v235
	v_cvt_pk_f16_f32 v174, v232, v233
	v_cvt_pk_f16_f32 v175, v236, v237
	v_cvt_pk_f16_f32 v176, v238, v239
	v_cvt_pk_f16_f32 v177, v242, v243
	v_cvt_pk_f16_f32 v178, v240, v241
	v_cvt_pk_f16_f32 v179, v244, v245
	s_mov_b32 s93, 1

.LBB5_42:
	s_and_b64 vcc, exec, s[4:5]
	s_cbranch_vccz .LBB5_3
	s_load_dwordx2 s[0:1], s[22:23], 0x18
	s_waitcnt lgkmcnt(0)
	s_load_dwordx2 s[6:7], s[0:1], 0x0
	s_load_dword s28, s[0:1], 0x8
	v_cmp_lt_u32_e64 s[64:65], 0, v182
	v_cmp_gt_u32_e64 s[66:67], 63, v182
	v_cmp_lt_u32_e64 s[68:69], 0, v162
	v_cmp_gt_u32_e64 s[70:71], 60, v162
	buffer_load_dwordx4 v[184:187], v180, s[16:19], 0 offen
	s_and_b64 s[72:73], s[68:69], s[64:65]
	s_and_b64 s[74:75], s[68:69], s[66:67]
	s_and_b64 s[76:77], s[70:71], s[64:65]
	s_and_b64 s[78:79], s[70:71], s[66:67]
	v_add_u32_e32 v224, 0xfffe7c00, v180
	v_add_u32_e32 v225, 0xfffe8000, v180
	s_mov_b64 exec, s[72:73]
	buffer_load_dwordx4 v[110:113], v224, s[16:19], 0 offen
	buffer_load_dwordx4 v[78:81], v224, s[16:19], 0 offen offset:512
	s_mov_b64 exec, -1
	s_mov_b64 exec, s[68:69]
	buffer_load_dwordx4 v[126:129], v225, s[16:19], 0 offen offset:512
	buffer_load_dwordx4 v[102:105], v225, s[16:19], 0 offen offset:1024
	s_mov_b64 exec, -1
	s_mov_b64 exec, s[74:75]
	buffer_load_dwordx4 v[134:137], v225, s[16:19], 0 offen offset:2048
	buffer_load_dwordx4 v[114:117], v225, s[16:19], 0 offen offset:2560
	s_mov_b64 exec, -1
	v_add_u32_e32 v224, 0xfffffc00, v180
	s_mov_b64 exec, s[64:65]
	buffer_load_dwordx4 v[82:85], v224, s[16:19], 0 offen
	buffer_load_dwordx4 v[42:45], v224, s[16:19], 0 offen offset:512
	s_mov_b64 exec, -1
	buffer_load_dwordx4 v[106:109], v180, s[16:19], 0 offen offset:512
	buffer_load_dwordx4 v[62:65], v180, s[16:19], 0 offen offset:1024
	s_mov_b64 exec, s[66:67]
	buffer_load_dwordx4 v[122:125], v180, s[16:19], 0 offen offset:2048
	buffer_load_dwordx4 v[86:89], v180, s[16:19], 0 offen offset:2560
	s_mov_b64 exec, -1
	v_add_u32_e32 v224, 0x17c00, v180
	v_add_u32_e32 v225, 0x18000, v180
	s_mov_b64 exec, s[64:65]
	buffer_load_dwordx4 v[50:53], v224, s[16:19], 0 offen
	buffer_load_dwordx4 v[22:25], v224, s[16:19], 0 offen offset:512
	s_mov_b64 exec, -1
	buffer_load_dwordx4 v[66:69], v225, s[16:19], 0 offen offset:512
	buffer_load_dwordx4 v[34:37], v225, s[16:19], 0 offen offset:1024
	s_mov_b64 exec, s[66:67]
	buffer_load_dwordx4 v[94:97], v225, s[16:19], 0 offen offset:2048
	buffer_load_dwordx4 v[46:49], v225, s[16:19], 0 offen offset:2560
	s_mov_b64 exec, -1
	v_add_u32_e32 v224, 0x18000, v180
	buffer_load_dwordx4 v[154:157], v224, s[16:19], 0 offen
	v_add_u32_e32 v225, 0x30000, v180
	buffer_load_dwordx4 v[150:153], v225, s[16:19], 0 offen
	v_add_u32_e32 v224, 0x48000, v180
	buffer_load_dwordx4 v[146:149], v224, s[16:19], 0 offen
	v_add_u32_e32 v224, 0x2fc00, v180
	v_add_u32_e32 v225, 0x30000, v180
	v_add_u32_e32 v226, 0x47c00, v180
	v_add_u32_e32 v227, 0x48000, v180
	v_add_u32_e32 v228, 0x5fc00, v180
	v_add_u32_e32 v229, 0x60000, v180
	s_cmp_lg_u32 s93, 0
	s_cbranch_scc1 .Lmybg_D2
	s_waitcnt vmcnt(22)
	v_cvt_pk_f16_f32 v172, v230, v231
	v_cvt_pk_f16_f32 v173, v234, v235
	v_cvt_pk_f16_f32 v174, v232, v233
	v_cvt_pk_f16_f32 v175, v236, v237
	v_cvt_pk_f16_f32 v176, v238, v239
	v_cvt_pk_f16_f32 v177, v242, v243
	v_cvt_pk_f16_f32 v178, v240, v241
	v_cvt_pk_f16_f32 v179, v244, v245
	s_mov_b32 s93, 1

	.amdhsa_kernel _Z7k_stageILi0ELi4EEv8AttnArgsPKDF16_PKfPDF16_iii
		.amdhsa_group_segment_fixed_size 82944
		.amdhsa_private_segment_fixed_size 0
		.amdhsa_kernarg_size 148
		.amdhsa_user_sgpr_count 2
		.amdhsa_user_sgpr_dispatch_ptr 0
		.amdhsa_user_sgpr_queue_ptr 0
		.amdhsa_user_sgpr_kernarg_segment_ptr 1
		.amdhsa_user_sgpr_dispatch_id 0
		.amdhsa_user_sgpr_kernarg_preload_length 0
		.amdhsa_user_sgpr_kernarg_preload_offset 0
		.amdhsa_user_sgpr_private_segment_size 0
		.amdhsa_uses_dynamic_stack 0
		.amdhsa_enable_private_segment 0
		.amdhsa_system_sgpr_workgroup_id_x 1
		.amdhsa_system_sgpr_workgroup_id_y 1
		.amdhsa_system_sgpr_workgroup_id_z 0
		.amdhsa_system_sgpr_workgroup_info 0
		.amdhsa_system_vgpr_workitem_id 0
		.amdhsa_next_free_vgpr 246
		.amdhsa_next_free_sgpr 96
		.amdhsa_accum_offset 248
		.amdhsa_reserve_vcc 1
		.amdhsa_float_round_mode_32 0
		.amdhsa_float_round_mode_16_64 0
		.amdhsa_float_denorm_mode_32 3
		.amdhsa_float_denorm_mode_16_64 3
		.amdhsa_dx10_clamp 1
		.amdhsa_ieee_mode 1
		.amdhsa_fp16_overflow 0
		.amdhsa_tg_split 0
		.amdhsa_exception_fp_ieee_invalid_op 0
		.amdhsa_exception_fp_denorm_src 0
		.amdhsa_exception_fp_ieee_div_zero 0
		.amdhsa_exception_fp_ieee_overflow 0
		.amdhsa_exception_fp_ieee_underflow 0
		.amdhsa_exception_fp_ieee_inexact 0
		.amdhsa_exception_int_div_zero 0
	.end_amdhsa_kernel

_Z7k_attn2ILi2EEv8AttnArgs:
	v_readfirstlane_b32 s3, v0
	s_lshl_b32 s12, s3, 1
	v_lshlrev_b32_e32 v3, 3, v0
	s_and_b32 s12, s12, 0x80
	v_and_b32_e32 v3, 0x78, v3
	s_load_dwordx4 s[8:11], s[0:1], 0x0
	s_load_dwordx2 s[4:5], s[0:1], 0x10
	s_load_dwordx2 s[6:7], s[0:1], 0x50
	v_or_b32_e32 v180, s12, v3
	s_lshl_b32 s12, s2, 5
	v_lshrrev_b32_e32 v1, 5, v0
	v_bfe_u32 v2, v0, 4, 2
	s_and_b32 s14, s12, 0xe0
	s_lshr_b32 s12, s2, 3
	v_lshrrev_b32_e32 v0, 6, v0
	v_and_b32_e32 v1, 4, v1
	s_add_i32 s14, s14, s12
	s_and_b32 s2, s2, 56
	v_and_b32_e32 v0, 4, v0
	v_and_or_b32 v181, s14, 56, v0
	v_or3_b32 v182, v2, s2, v1
	s_and_b32 s2, s14, 0x3ffffc0
	v_or_b32_e32 v4, s2, v181
	v_lshlrev_b32_e32 v0, 1, v180
	v_mov_b32_e32 v1, 0
	s_waitcnt lgkmcnt(0)
	v_lshl_add_u64 v[2:3], s[6:7], 0, v[0:1]
	v_lshl_or_b32 v0, v4, 6, v182
	v_lshlrev_b64 v[4:5], 9, v[0:1]
	v_lshl_add_u64 v[8:9], v[2:3], 0, v[4:5]
	v_or_b32_e32 v4, 64, v0
	v_mov_b32_e32 v5, v1
	v_lshlrev_b64 v[4:5], 9, v[4:5]
	v_lshlrev_b32_e32 v20, 2, v180
	v_lshl_add_u64 v[10:11], v[2:3], 0, v[4:5]
	global_load_dwordx4 v[240:243], v20, s[10:11] offset:16
	global_load_dwordx4 v[236:239], v20, s[10:11]
	global_load_dwordx4 v[248:251], v20, s[4:5] offset:16
	global_load_dwordx4 v[244:247], v20, s[4:5]
	global_load_dwordx4 v[12:15], v[8:9], off nt
	global_load_dwordx4 v[4:7], v[10:11], off nt
	v_or_b32_e32 v8, 0x80, v0
	v_mov_b32_e32 v9, v1
	v_lshlrev_b64 v[8:9], 9, v[8:9]
	v_or_b32_e32 v0, 0xc0, v0
	v_lshl_add_u64 v[20:21], v[2:3], 0, v[8:9]
	v_lshlrev_b64 v[0:1], 9, v[0:1]
	v_lshl_add_u64 v[34:35], v[2:3], 0, v[0:1]
	global_load_dwordx4 v[8:11], v[20:21], off nt
	global_load_dwordx4 v[0:3], v[34:35], off nt
	s_bitcmp1_b32 s3, 6
	s_cselect_b64 s[4:5], -1, 0
	s_and_b32 s2, s14, 0x3ffc0
	v_or_b32_e32 v20, s2, v181
	v_lshl_or_b32 v20, v20, 6, v182
	v_add_u32_e32 v184, -1, v182
	v_add_u32_e32 v185, -1, v181
	v_mul_u32_u24_e32 v20, 0x300, v20
	v_or_b32_e32 v34, v185, v184
	v_or_b32_e32 v20, v180, v20
	s_mov_b32 s11, 0x20000
	s_mov_b32 s10, 0x1800000
	s_and_b32 s9, s9, 0xffff
	v_lshlrev_b32_e32 v183, 1, v20
	v_cmp_gt_u32_e64 s[2:3], 64, v34
	s_and_b64 vcc, exec, s[4:5]
	s_cbranch_vccz .LBB6_38
	s_load_dwordx2 s[12:13], s[0:1], 0x20
	s_waitcnt lgkmcnt(0)
	s_load_dwordx2 s[4:5], s[12:13], 0x0
	s_load_dword s12, s[12:13], 0x8
	v_cmp_lt_u32_e64 s[64:65], 0, v182
	v_cmp_gt_u32_e64 s[66:67], 63, v182
	v_cmp_lt_u32_e64 s[68:69], 0, v181
	v_cmp_gt_u32_e64 s[70:71], 60, v181
	buffer_load_dwordx4 v[190:193], v183, s[8:11], 0 offen
	s_and_b64 s[72:73], s[68:69], s[64:65]
	s_and_b64 s[74:75], s[68:69], s[66:67]
	s_and_b64 s[76:77], s[70:71], s[64:65]
	s_and_b64 s[78:79], s[70:71], s[66:67]
	v_add_u32_e32 v228, 0xfffe7c00, v183
	v_add_u32_e32 v229, 0xfffe8000, v183
	s_mov_b64 exec, s[72:73]
	buffer_load_dwordx4 v[136:139], v228, s[8:11], 0 offen
	buffer_load_dwordx4 v[96:99], v228, s[8:11], 0 offen offset:512
	s_mov_b64 exec, -1
	s_mov_b64 exec, s[68:69]
	buffer_load_dwordx4 v[152:155], v229, s[8:11], 0 offen offset:512
	buffer_load_dwordx4 v[124:127], v229, s[8:11], 0 offen offset:1024
	s_mov_b64 exec, -1
	s_mov_b64 exec, s[74:75]
	buffer_load_dwordx4 v[160:163], v229, s[8:11], 0 offen offset:2048
	buffer_load_dwordx4 v[140:143], v229, s[8:11], 0 offen offset:2560
	s_mov_b64 exec, -1
	v_add_u32_e32 v228, 0xfffffc00, v183
	s_mov_b64 exec, s[64:65]
	buffer_load_dwordx4 v[112:115], v228, s[8:11], 0 offen
	buffer_load_dwordx4 v[68:71], v228, s[8:11], 0 offen offset:512
	s_mov_b64 exec, -1
	buffer_load_dwordx4 v[132:135], v183, s[8:11], 0 offen offset:512
	buffer_load_dwordx4 v[88:91], v183, s[8:11], 0 offen offset:1024
	s_mov_b64 exec, s[66:67]
	buffer_load_dwordx4 v[148:151], v183, s[8:11], 0 offen offset:2048
	buffer_load_dwordx4 v[108:111], v183, s[8:11], 0 offen offset:2560
	s_mov_b64 exec, -1
	v_add_u32_e32 v228, 0x17c00, v183
	v_add_u32_e32 v229, 0x18000, v183
	s_mov_b64 exec, s[64:65]
	buffer_load_dwordx4 v[76:79], v228, s[8:11], 0 offen
	buffer_load_dwordx4 v[48:51], v228, s[8:11], 0 offen offset:512
	s_mov_b64 exec, -1
	buffer_load_dwordx4 v[92:95], v229, s[8:11], 0 offen offset:512
	buffer_load_dwordx4 v[56:59], v229, s[8:11], 0 offen offset:1024
	s_mov_b64 exec, s[66:67]
	buffer_load_dwordx4 v[116:119], v229, s[8:11], 0 offen offset:2048
	buffer_load_dwordx4 v[72:75], v229, s[8:11], 0 offen offset:2560
	s_mov_b64 exec, -1
	v_add_u32_e32 v228, 0x18000, v183
	buffer_load_dwordx4 v[176:179], v228, s[8:11], 0 offen
	v_add_u32_e32 v229, 0x30000, v183
	buffer_load_dwordx4 v[172:175], v229, s[8:11], 0 offen
	v_add_u32_e32 v228, 0x48000, v183
	buffer_load_dwordx4 v[168:171], v228, s[8:11], 0 offen
	v_add_u32_e32 v228, 0x2fc00, v183
	v_add_u32_e32 v229, 0x30000, v183
	v_add_u32_e32 v230, 0x47c00, v183
	v_add_u32_e32 v231, 0x48000, v183
	v_add_u32_e32 v232, 0x5fc00, v183
	v_add_u32_e32 v233, 0x60000, v183
	s_waitcnt vmcnt(26)
	v_cvt_pk_f16_f32 v22, v240, v241
	v_cvt_pk_f16_f32 v20, v236, v237
	v_cvt_pk_f16_f32 v21, v238, v239
	v_cvt_pk_f16_f32 v16, v244, v245
	v_cvt_pk_f16_f32 v17, v246, v247
	v_cvt_pk_f16_f32 v18, v248, v249
	v_cvt_pk_f16_f32 v23, v242, v243
	v_cvt_pk_f16_f32 v19, v250, v251
	s_not_b64 exec, s[72:73]
	s_cbranch_execz .Lmyf_E1_0
	v_mov_b32_e32 v136, v20
	v_mov_b32_e32 v137, v21
	v_mov_b32_e32 v138, v22
	v_mov_b32_e32 v139, v23
	v_mov_b32_e32 v96, v16
	v_mov_b32_e32 v97, v17
	v_mov_b32_e32 v98, v18
	v_mov_b32_e32 v99, v19

.LBB6_38:
	s_load_dwordx2 s[12:13], s[0:1], 0x60
	s_cbranch_execz .LBB6_76
	s_load_dwordx2 s[2:3], s[0:1], 0x18
	s_waitcnt lgkmcnt(0)
	s_load_dwordx2 s[0:1], s[2:3], 0x0
	s_load_dword s4, s[2:3], 0x8
	v_cmp_lt_u32_e64 s[64:65], 0, v182
	v_cmp_gt_u32_e64 s[66:67], 63, v182
	v_cmp_lt_u32_e64 s[68:69], 0, v181
	v_cmp_gt_u32_e64 s[70:71], 60, v181
	buffer_load_dwordx4 v[168:171], v183, s[8:11], 0 offen
	s_and_b64 s[72:73], s[68:69], s[64:65]
	s_and_b64 s[74:75], s[68:69], s[66:67]
	s_and_b64 s[76:77], s[70:71], s[64:65]
	s_and_b64 s[78:79], s[70:71], s[66:67]
	v_add_u32_e32 v228, 0xfffe7c00, v183
	v_add_u32_e32 v229, 0xfffe8000, v183
	s_mov_b64 exec, s[72:73]
	buffer_load_dwordx4 v[140:143], v228, s[8:11], 0 offen
	buffer_load_dwordx4 v[120:123], v228, s[8:11], 0 offen offset:512
	s_mov_b64 exec, -1
	s_mov_b64 exec, s[68:69]
	buffer_load_dwordx4 v[152:155], v229, s[8:11], 0 offen offset:512
	buffer_load_dwordx4 v[132:135], v229, s[8:11], 0 offen offset:1024
	s_mov_b64 exec, -1
	s_mov_b64 exec, s[74:75]
	buffer_load_dwordx4 v[156:159], v229, s[8:11], 0 offen offset:2048
	buffer_load_dwordx4 v[144:147], v229, s[8:11], 0 offen offset:2560
	s_mov_b64 exec, -1
	v_add_u32_e32 v228, 0xfffffc00, v183
	s_mov_b64 exec, s[64:65]
	buffer_load_dwordx4 v[124:127], v228, s[8:11], 0 offen
	buffer_load_dwordx4 v[104:107], v228, s[8:11], 0 offen offset:512
	s_mov_b64 exec, -1
	buffer_load_dwordx4 v[136:139], v183, s[8:11], 0 offen offset:512
	buffer_load_dwordx4 v[108:111], v183, s[8:11], 0 offen offset:1024
	s_mov_b64 exec, s[66:67]
	buffer_load_dwordx4 v[148:151], v183, s[8:11], 0 offen offset:2048
	buffer_load_dwordx4 v[88:91], v183, s[8:11], 0 offen offset:2560
	s_mov_b64 exec, -1
	v_add_u32_e32 v228, 0x17c00, v183
	v_add_u32_e32 v229, 0x18000, v183
	s_mov_b64 exec, s[64:65]
	buffer_load_dwordx4 v[64:67], v228, s[8:11], 0 offen
	buffer_load_dwordx4 v[40:43], v228, s[8:11], 0 offen offset:512
	s_mov_b64 exec, -1
	buffer_load_dwordx4 v[76:79], v229, s[8:11], 0 offen offset:512
	buffer_load_dwordx4 v[48:51], v229, s[8:11], 0 offen offset:1024
	s_mov_b64 exec, s[66:67]
	buffer_load_dwordx4 v[92:95], v229, s[8:11], 0 offen offset:2048
	buffer_load_dwordx4 v[60:63], v229, s[8:11], 0 offen offset:2560
	s_mov_b64 exec, -1
	v_add_u32_e32 v228, 0x2fc00, v183
	v_add_u32_e32 v229, 0x30000, v183
	s_mov_b64 exec, s[64:65]
	buffer_load_dwordx4 v[36:39], v228, s[8:11], 0 offen
	buffer_load_dwordx4 v[24:27], v228, s[8:11], 0 offen offset:512
	s_mov_b64 exec, -1
	buffer_load_dwordx4 v[52:55], v229, s[8:11], 0 offen offset:512
	buffer_load_dwordx4 v[28:31], v229, s[8:11], 0 offen offset:1024
	s_mov_b64 exec, s[66:67]
	buffer_load_dwordx4 v[68:71], v229, s[8:11], 0 offen offset:2048
	buffer_load_dwordx4 v[32:35], v229, s[8:11], 0 offen offset:2560
	s_mov_b64 exec, -1
	v_add_u32_e32 v228, 0x18000, v183
	buffer_load_dwordx4 v[160:163], v228, s[8:11], 0 offen
	v_add_u32_e32 v228, 0x47c00, v183
	v_add_u32_e32 v229, 0x48000, v183
	v_add_u32_e32 v230, 0x5fc00, v183
	v_add_u32_e32 v231, 0x60000, v183
	s_waitcnt vmcnt(30)
	v_cvt_pk_f16_f32 v22, v240, v241
	v_cvt_pk_f16_f32 v20, v236, v237
	v_cvt_pk_f16_f32 v21, v238, v239
	v_cvt_pk_f16_f32 v16, v244, v245
	v_cvt_pk_f16_f32 v17, v246, v247
	v_cvt_pk_f16_f32 v18, v248, v249
	v_cvt_pk_f16_f32 v23, v242, v243
	v_cvt_pk_f16_f32 v19, v250, v251
	s_not_b64 exec, s[72:73]
	s_cbranch_execz .Lmyf_E2_0
	v_mov_b32_e32 v140, v20
	v_mov_b32_e32 v141, v21
	v_mov_b32_e32 v142, v22
	v_mov_b32_e32 v143, v23
	v_mov_b32_e32 v120, v16
	v_mov_b32_e32 v121, v17
	v_mov_b32_e32 v122, v18
	v_mov_b32_e32 v123, v19

	.amdhsa_kernel _Z7k_attn2ILi2EEv8AttnArgs
		.amdhsa_group_segment_fixed_size 0
		.amdhsa_private_segment_fixed_size 0
		.amdhsa_kernarg_size 112
		.amdhsa_user_sgpr_count 2
		.amdhsa_user_sgpr_dispatch_ptr 0
		.amdhsa_user_sgpr_queue_ptr 0
		.amdhsa_user_sgpr_kernarg_segment_ptr 1
		.amdhsa_user_sgpr_dispatch_id 0
		.amdhsa_user_sgpr_kernarg_preload_length 0
		.amdhsa_user_sgpr_kernarg_preload_offset 0
		.amdhsa_user_sgpr_private_segment_size 0
		.amdhsa_uses_dynamic_stack 0
		.amdhsa_enable_private_segment 0
		.amdhsa_system_sgpr_workgroup_id_x 1
		.amdhsa_system_sgpr_workgroup_id_y 0
		.amdhsa_system_sgpr_workgroup_id_z 0
		.amdhsa_system_sgpr_workgroup_info 0
		.amdhsa_system_vgpr_workitem_id 0
		.amdhsa_next_free_vgpr 252
		.amdhsa_next_free_sgpr 96
		.amdhsa_accum_offset 252
		.amdhsa_reserve_vcc 1
		.amdhsa_float_round_mode_32 0
		.amdhsa_float_round_mode_16_64 0
		.amdhsa_float_denorm_mode_32 3
		.amdhsa_float_denorm_mode_16_64 3
		.amdhsa_dx10_clamp 1
		.amdhsa_ieee_mode 1
		.amdhsa_fp16_overflow 0
		.amdhsa_tg_split 0
		.amdhsa_exception_fp_ieee_invalid_op 0
		.amdhsa_exception_fp_denorm_src 0
		.amdhsa_exception_fp_ieee_div_zero 0
		.amdhsa_exception_fp_ieee_overflow 0
		.amdhsa_exception_fp_ieee_underflow 0
		.amdhsa_exception_fp_ieee_inexact 0
		.amdhsa_exception_int_div_zero 0
	.end_amdhsa_kernel

amdhsa.kernels:
  - .agpr_count:     0
    .args:
      - .actual_access:  read_only
        .address_space:  global
        .offset:         0
        .size:           8
        .value_kind:     global_buffer
      - .actual_access:  read_only
        .address_space:  global
        .offset:         8
        .size:           8
        .value_kind:     global_buffer
      - .actual_access:  read_only
        .address_space:  global
        .offset:         16
        .size:           8
        .value_kind:     global_buffer
      - .actual_access:  read_only
        .address_space:  global
        .offset:         24
        .size:           8
        .value_kind:     global_buffer
      - .actual_access:  read_only
        .address_space:  global
        .offset:         32
        .size:           8
        .value_kind:     global_buffer
      - .actual_access:  read_only
        .address_space:  global
        .offset:         40
        .size:           8
        .value_kind:     global_buffer
      - .actual_access:  read_only
        .address_space:  global
        .offset:         48
        .size:           8
        .value_kind:     global_buffer
      - .actual_access:  read_only
        .address_space:  global
        .offset:         56
        .size:           8
        .value_kind:     global_buffer
      - .actual_access:  write_only
        .address_space:  global
        .offset:         64
        .size:           8
        .value_kind:     global_buffer
      - .actual_access:  write_only
        .address_space:  global
        .offset:         72
        .size:           8
        .value_kind:     global_buffer
      - .actual_access:  write_only
        .address_space:  global
        .offset:         80
        .size:           8
        .value_kind:     global_buffer
      - .actual_access:  write_only
        .address_space:  global
        .offset:         88
        .size:           8
        .value_kind:     global_buffer
    .group_segment_fixed_size: 0
    .kernarg_segment_align: 8
    .kernarg_segment_size: 96
    .language:       OpenCL C
    .language_version:
      - 2
      - 0
    .max_flat_workgroup_size: 256
    .name:           _Z8k_prep_wPKfS0_S0_S0_S0_S0_S0_S0_PDF16_PfS1_S1_
    .private_segment_fixed_size: 0
    .sgpr_count:     23
    .sgpr_spill_count: 0
    .symbol:         _Z8k_prep_wPKfS0_S0_S0_S0_S0_S0_S0_PDF16_PfS1_S1_.kd
    .uniform_work_group_size: 1
    .uses_dynamic_stack: false
    .vgpr_count:     15
    .vgpr_spill_count: 0
    .wavefront_size: 64
  - .agpr_count:     0
    .args:
      - .actual_access:  read_only
        .address_space:  global
        .offset:         0
        .size:           8
        .value_kind:     global_buffer
      - .actual_access:  read_only
        .address_space:  global
        .offset:         8
        .size:           8
        .value_kind:     global_buffer
      - .actual_access:  read_only
        .address_space:  global
        .offset:         16
        .size:           8
        .value_kind:     global_buffer
      - .actual_access:  read_only
        .address_space:  global
        .offset:         24
        .size:           8
        .value_kind:     global_buffer
      - .actual_access:  write_only
        .address_space:  global
        .offset:         32
        .size:           8
        .value_kind:     global_buffer
      - .actual_access:  read_only
        .address_space:  global
        .offset:         40
        .size:           8
        .value_kind:     global_buffer
      - .actual_access:  read_only
        .address_space:  global
        .offset:         48
        .size:           8
        .value_kind:     global_buffer
      - .actual_access:  write_only
        .address_space:  global
        .offset:         56
        .size:           8
        .value_kind:     global_buffer
      - .offset:         64
        .size:           4
        .value_kind:     by_value
      - .offset:         68
        .size:           4
        .value_kind:     by_value
    .group_segment_fixed_size: 115712
    .kernarg_segment_align: 8
    .kernarg_segment_size: 72
    .language:       OpenCL C
    .language_version:
      - 2
      - 0
    .max_flat_workgroup_size: 512
    .name:           _Z8k_stageAPKfS0_S0_S0_PDF16_PKDF16_S0_S1_ii
    .private_segment_fixed_size: 0
    .sgpr_count:     28
    .sgpr_spill_count: 0
    .symbol:         _Z8k_stageAPKfS0_S0_S0_PDF16_PKDF16_S0_S1_ii.kd
    .uniform_work_group_size: 1
    .uses_dynamic_stack: false
    .vgpr_count:     251
    .vgpr_spill_count: 0
    .wavefront_size: 64
  - .agpr_count:     112
    .args:
      - .actual_access:  read_only
        .address_space:  global
        .offset:         0
        .size:           8
        .value_kind:     global_buffer
      - .actual_access:  read_only
        .address_space:  global
        .offset:         8
        .size:           8
        .value_kind:     global_buffer
      - .actual_access:  read_only
        .address_space:  global
        .offset:         16
        .size:           8
        .value_kind:     global_buffer
      - .actual_access:  read_only
        .address_space:  global
        .offset:         24
        .size:           8
        .value_kind:     global_buffer
      - .actual_access:  read_only
        .address_space:  global
        .offset:         32
        .size:           8
        .value_kind:     global_buffer
      - .actual_access:  write_only
        .address_space:  global
        .offset:         40
        .size:           8
        .value_kind:     global_buffer
    .group_segment_fixed_size: 107712
    .kernarg_segment_align: 8
    .kernarg_segment_size: 48
    .language:       OpenCL C
    .language_version:
      - 2
      - 0
    .max_flat_workgroup_size: 256
    .name:           _Z7k_conv4PKDF16_S0_S0_PKfS2_Pf
    .private_segment_fixed_size: 0
    .sgpr_count:     36
    .sgpr_spill_count: 0
    .symbol:         _Z7k_conv4PKDF16_S0_S0_PKfS2_Pf.kd
    .uniform_work_group_size: 1
    .uses_dynamic_stack: false
    .vgpr_count:     328
    .vgpr_spill_count: 0
    .wavefront_size: 64
  - .agpr_count:     0
    .args:
      - .offset:         0
        .size:           112
        .value_kind:     by_value
      - .actual_access:  read_only
        .address_space:  global
        .offset:         112
        .size:           8
        .value_kind:     global_buffer
      - .actual_access:  read_only
        .address_space:  global
        .offset:         120
        .size:           8
        .value_kind:     global_buffer
      - .actual_access:  write_only
        .address_space:  global
        .offset:         128
        .size:           8
        .value_kind:     global_buffer
      - .offset:         136
        .size:           4
        .value_kind:     by_value
      - .offset:         140
        .size:           4
        .value_kind:     by_value
      - .offset:         144
        .size:           4
        .value_kind:     by_value
    .group_segment_fixed_size: 115712
    .kernarg_segment_align: 8
    .kernarg_segment_size: 148
    .language:       OpenCL C
    .language_version:
      - 2
      - 0
    .max_flat_workgroup_size: 512
    .name:           _Z7k_stageILi0ELi8EEv8AttnArgsPKDF16_PKfPDF16_iii
    .private_segment_fixed_size: 0
    .sgpr_count:     41
    .sgpr_spill_count: 0
    .symbol:         _Z7k_stageILi0ELi8EEv8AttnArgsPKDF16_PKfPDF16_iii.kd
    .uniform_work_group_size: 1
    .uses_dynamic_stack: false
    .vgpr_count:     255
    .vgpr_spill_count: 0
    .wavefront_size: 64
  - .agpr_count:     0
    .args:
      - .offset:         0
        .size:           112
        .value_kind:     by_value
      - .actual_access:  read_only
        .address_space:  global
        .offset:         112
        .size:           8
        .value_kind:     global_buffer
      - .actual_access:  read_only
        .address_space:  global
        .offset:         120
        .size:           8
        .value_kind:     global_buffer
      - .actual_access:  write_only
        .address_space:  global
        .offset:         128
        .size:           8
        .value_kind:     global_buffer
      - .offset:         136
        .size:           4
        .value_kind:     by_value
      - .offset:         140
        .size:           4
        .value_kind:     by_value
      - .offset:         144
        .size:           4
        .value_kind:     by_value
    .group_segment_fixed_size: 82944
    .kernarg_segment_align: 8
    .kernarg_segment_size: 148
    .language:       OpenCL C
    .language_version:
      - 2
      - 0
    .max_flat_workgroup_size: 512
    .name:           _Z7k_stageILi1ELi4EEv8AttnArgsPKDF16_PKfPDF16_iii
    .private_segment_fixed_size: 0
    .sgpr_count:     55
    .sgpr_spill_count: 0
    .symbol:         _Z7k_stageILi1ELi4EEv8AttnArgsPKDF16_PKfPDF16_iii.kd
    .uniform_work_group_size: 1
    .uses_dynamic_stack: false
    .vgpr_count:     252
    .vgpr_spill_count: 0
    .wavefront_size: 64
  - .agpr_count:     0
    .args:
      - .offset:         0
        .size:           112
        .value_kind:     by_value
      - .actual_access:  read_only
        .address_space:  global
        .offset:         112
        .size:           8
        .value_kind:     global_buffer
      - .actual_access:  read_only
        .address_space:  global
        .offset:         120
        .size:           8
        .value_kind:     global_buffer
      - .actual_access:  write_only
        .address_space:  global
        .offset:         128
        .size:           8
        .value_kind:     global_buffer
      - .offset:         136
        .size:           4
        .value_kind:     by_value
      - .offset:         140
        .size:           4
        .value_kind:     by_value
      - .offset:         144
        .size:           4
        .value_kind:     by_value
    .group_segment_fixed_size: 82944
    .kernarg_segment_align: 8
    .kernarg_segment_size: 148
    .language:       OpenCL C
    .language_version:
      - 2
      - 0
    .max_flat_workgroup_size: 512
    .name:           _Z7k_stageILi0ELi4EEv8AttnArgsPKDF16_PKfPDF16_iii
    .private_segment_fixed_size: 0
    .sgpr_count:     38
    .sgpr_spill_count: 0
    .symbol:         _Z7k_stageILi0ELi4EEv8AttnArgsPKDF16_PKfPDF16_iii.kd
    .uniform_work_group_size: 1
    .uses_dynamic_stack: false
    .vgpr_count:     246
    .vgpr_spill_count: 0
    .wavefront_size: 64
  - .agpr_count:     0
    .args:
      - .offset:         0
        .size:           112
        .value_kind:     by_value
    .group_segment_fixed_size: 0
    .kernarg_segment_align: 8
    .kernarg_segment_size: 112
    .language:       OpenCL C
    .language_version:
      - 2
      - 0
    .max_flat_workgroup_size: 512
    .name:           _Z7k_attn2ILi2EEv8AttnArgs
    .private_segment_fixed_size: 0
    .sgpr_count:     102
    .sgpr_spill_count: 0
    .symbol:         _Z7k_attn2ILi2EEv8AttnArgs.kd
    .uniform_work_group_size: 1
    .uses_dynamic_stack: false
    .vgpr_count:     252
    .vgpr_spill_count: 0
    .wavefront_size: 64
